# v47 plus non-temporal loads of the residual input x in the w_o GEMM epilogue
# baseline (speedup 1.0000x reference)
;     template <class U> __device__ __forceinline__ void operator()(const f32x4 (&acc)[2][2][4][2], const U& u, int wr, int wc, int fr, int fq) const {
;         const int row0 = u.orow0 + wr * 64 + fr, col0 = u.ocol0 + wc * 32 + 4 * fq; const int b = u.orow0 >> 12;
;         f32x4 gv[2][2];
; #pragma unroll
;         for (int bj = 0; bj < 2; ++bj)
; #pragma unroll
;             for (int n = 0; n < 2; ++n) gv[bj][n] = *(const f32x4*)(gate + (size_t)b * ADA_W + col0 + bj * HALF + 16 * n) + 1.0f;
; #pragma unroll
;         for (int ai = 0; ai < 2; ++ai)
; #pragma unroll
;             for (int m = 0; m < 4; ++m) { const size_t ro = (size_t)(row0 + ai * HALF + m * 16) * DM + col0;
; #pragma unroll
;                 for (int bj = 0; bj < 2; ++bj)
; #pragma unroll
;                     for (int n = 0; n < 2; ++n) { const f32x4 xv = *(const f32x4*)(X + ro + bj * HALF + 16 * n);
;                         *(f32x4*)(Y + ro + bj * HALF + 16 * n) = xv * DN_ALPHA + gv[bj][n] * acc[ai][bj][m][n]; } }
;     }
.LBB0_969:
	s_ashr_i32 s0, s33, 12
	s_mul_hi_i32 s1, s0, 0xc000
	s_mul_i32 s0, s0, 0xc000
	v_add_u32_e32 v148, s51, v232
	s_add_u32 s0, s43, s0
	s_addc_u32 s1, s44, s1
	v_ashrrev_i32_e32 v149, 31, v148
	v_lshl_add_u64 v[144:145], v[148:149], 2, s[0:1]
	global_load_dwordx4 v[128:131], v[144:145], off
	s_mov_b32 s22, 0x3fb504f3
	s_mov_b64 s[0:1], 0x20000
	s_and_b64 vcc, exec, s[18:19]
	s_mov_b32 s51, s50
	s_mov_b64 s[24:25], s[20:21]
	s_waitcnt vmcnt(0)
	v_pk_add_f32 v[140:141], v[130:131], 1.0 op_sel_hi:[1,0]
	v_pk_add_f32 v[142:143], v[128:129], 1.0 op_sel_hi:[1,0]
	global_load_dwordx4 v[128:131], v[144:145], off offset:64
	s_waitcnt vmcnt(0)
	v_pk_add_f32 v[136:137], v[130:131], 1.0 op_sel_hi:[1,0]
	v_pk_add_f32 v[138:139], v[128:129], 1.0 op_sel_hi:[1,0]
	global_load_dwordx4 v[128:131], v[144:145], off offset:512
	s_waitcnt vmcnt(0)
	v_pk_add_f32 v[132:133], v[130:131], 1.0 op_sel_hi:[1,0]
	global_load_dwordx4 v[144:147], v[144:145], off offset:576
	v_pk_add_f32 v[134:135], v[128:129], 1.0 op_sel_hi:[1,0]
	s_waitcnt vmcnt(0)
	v_pk_add_f32 v[130:131], v[144:145], 1.0 op_sel_hi:[1,0]
	v_add_u32_e32 v144, s33, v218
	v_ashrrev_i32_e32 v145, 31, v144
	v_lshlrev_b64 v[144:145], 11, v[144:145]
	v_lshl_add_u64 v[144:145], v[144:145], 0, v[148:149]
	v_lshlrev_b64 v[144:145], 2, v[144:145]
	v_lshl_add_u64 v[150:151], s[4:5], 0, v[144:145]
	v_pk_add_f32 v[128:129], v[146:147], 1.0 op_sel_hi:[1,0]
	global_load_dwordx4 v[146:149], v[150:151], off nt
	s_mov_b32 s33, s49
	s_waitcnt vmcnt(0)
	v_pk_mul_f32 v[148:149], v[148:149], s[22:23] op_sel_hi:[1,0]
	v_pk_mul_f32 v[146:147], v[146:147], s[22:23] op_sel_hi:[1,0]
	v_pk_fma_f32 v[126:127], v[126:127], v[140:141], v[148:149]
	v_pk_fma_f32 v[124:125], v[124:125], v[142:143], v[146:147]
	v_lshl_add_u64 v[146:147], s[12:13], 0, v[144:145]
	global_store_dwordx4 v[146:147], v[124:127], off
	global_load_dwordx4 v[124:127], v[150:151], off offset:64 nt
	s_waitcnt vmcnt(0)
	v_pk_mul_f32 v[126:127], v[126:127], s[22:23] op_sel_hi:[1,0]
	v_pk_mul_f32 v[124:125], v[124:125], s[22:23] op_sel_hi:[1,0]
	v_pk_fma_f32 v[122:123], v[122:123], v[136:137], v[126:127]
	v_pk_fma_f32 v[120:121], v[120:121], v[138:139], v[124:125]
	global_store_dwordx4 v[146:147], v[120:123], off offset:64
	global_load_dwordx4 v[120:123], v[150:151], off offset:512 nt
	s_waitcnt vmcnt(0)
	v_pk_mul_f32 v[122:123], v[122:123], s[22:23] op_sel_hi:[1,0]
	v_pk_mul_f32 v[120:121], v[120:121], s[22:23] op_sel_hi:[1,0]
	v_pk_fma_f32 v[118:119], v[118:119], v[132:133], v[122:123]
	v_pk_fma_f32 v[116:117], v[116:117], v[134:135], v[120:121]
	global_store_dwordx4 v[146:147], v[116:119], off offset:512
	global_load_dwordx4 v[116:119], v[150:151], off offset:576 nt
	s_waitcnt vmcnt(0)
	v_pk_mul_f32 v[118:119], v[118:119], s[22:23] op_sel_hi:[1,0]
	v_pk_mul_f32 v[116:117], v[116:117], s[22:23] op_sel_hi:[1,0]
	v_pk_fma_f32 v[114:115], v[114:115], v[128:129], v[118:119]
	v_pk_fma_f32 v[112:113], v[112:113], v[130:131], v[116:117]
	v_lshl_add_u64 v[116:117], v[144:145], 0, s[0:1]
	global_store_dwordx4 v[146:147], v[112:115], off offset:576
	v_lshl_add_u64 v[118:119], s[4:5], 0, v[116:117]
	global_load_dwordx4 v[112:115], v[118:119], off nt
	s_mov_b64 s[0:1], 0x40000
	s_waitcnt vmcnt(0)
	v_pk_mul_f32 v[114:115], v[114:115], s[22:23] op_sel_hi:[1,0]
	v_pk_mul_f32 v[112:113], v[112:113], s[22:23] op_sel_hi:[1,0]
	v_pk_fma_f32 v[110:111], v[110:111], v[140:141], v[114:115]
	v_pk_fma_f32 v[108:109], v[108:109], v[142:143], v[112:113]
	v_lshl_add_u64 v[112:113], s[12:13], 0, v[116:117]
	global_store_dwordx4 v[112:113], v[108:111], off
	global_load_dwordx4 v[108:111], v[118:119], off offset:64 nt
	s_waitcnt vmcnt(0)
	v_pk_mul_f32 v[110:111], v[110:111], s[22:23] op_sel_hi:[1,0]
	v_pk_mul_f32 v[108:109], v[108:109], s[22:23] op_sel_hi:[1,0]
	v_pk_fma_f32 v[106:107], v[106:107], v[136:137], v[110:111]
	v_pk_fma_f32 v[104:105], v[104:105], v[138:139], v[108:109]
	global_store_dwordx4 v[112:113], v[104:107], off offset:64
	global_load_dwordx4 v[104:107], v[118:119], off offset:512 nt
	s_waitcnt vmcnt(0)
	v_pk_mul_f32 v[106:107], v[106:107], s[22:23] op_sel_hi:[1,0]
	v_pk_mul_f32 v[104:105], v[104:105], s[22:23] op_sel_hi:[1,0]
	v_pk_fma_f32 v[102:103], v[102:103], v[132:133], v[106:107]
	v_pk_fma_f32 v[100:101], v[100:101], v[134:135], v[104:105]
	global_store_dwordx4 v[112:113], v[100:103], off offset:512
	global_load_dwordx4 v[100:103], v[118:119], off offset:576 nt
	s_waitcnt vmcnt(0)
	v_pk_mul_f32 v[102:103], v[102:103], s[22:23] op_sel_hi:[1,0]
	v_pk_mul_f32 v[100:101], v[100:101], s[22:23] op_sel_hi:[1,0]
	v_pk_fma_f32 v[98:99], v[98:99], v[128:129], v[102:103]
	v_pk_fma_f32 v[96:97], v[96:97], v[130:131], v[100:101]
	v_lshl_add_u64 v[100:101], v[144:145], 0, s[0:1]
	global_store_dwordx4 v[112:113], v[96:99], off offset:576
	v_lshl_add_u64 v[102:103], s[4:5], 0, v[100:101]
	global_load_dwordx4 v[96:99], v[102:103], off nt
	s_mov_b64 s[0:1], 0x60000
	s_waitcnt vmcnt(0)
	v_pk_mul_f32 v[98:99], v[98:99], s[22:23] op_sel_hi:[1,0]
	v_pk_mul_f32 v[96:97], v[96:97], s[22:23] op_sel_hi:[1,0]
	v_pk_fma_f32 v[94:95], v[94:95], v[140:141], v[98:99]
	v_pk_fma_f32 v[92:93], v[92:93], v[142:143], v[96:97]
	v_lshl_add_u64 v[96:97], s[12:13], 0, v[100:101]
	global_store_dwordx4 v[96:97], v[92:95], off
	global_load_dwordx4 v[92:95], v[102:103], off offset:64 nt
	s_waitcnt vmcnt(0)
	v_pk_mul_f32 v[94:95], v[94:95], s[22:23] op_sel_hi:[1,0]
	v_pk_mul_f32 v[92:93], v[92:93], s[22:23] op_sel_hi:[1,0]
	v_pk_fma_f32 v[90:91], v[90:91], v[136:137], v[94:95]
	v_pk_fma_f32 v[88:89], v[88:89], v[138:139], v[92:93]
	global_store_dwordx4 v[96:97], v[88:91], off offset:64
	global_load_dwordx4 v[88:91], v[102:103], off offset:512 nt
	s_waitcnt vmcnt(0)
;     template <class U> __device__ __forceinline__ void operator()(const f32x4 (&acc)[2][2][4][2], const U& u, int wr, int wc, int fr, int fq) const {
;         const int row0 = u.orow0 + wr * 64 + fr, col0 = u.ocol0 + wc * 32 + 4 * fq; const int b = u.orow0 >> 12;
;         f32x4 gv[2][2];
; #pragma unroll
;         for (int bj = 0; bj < 2; ++bj)
; #pragma unroll
;             for (int n = 0; n < 2; ++n) gv[bj][n] = *(const f32x4*)(gate + (size_t)b * ADA_W + col0 + bj * HALF + 16 * n) + 1.0f;
; #pragma unroll
;         for (int ai = 0; ai < 2; ++ai)
; #pragma unroll
;             for (int m = 0; m < 4; ++m) { const size_t ro = (size_t)(row0 + ai * HALF + m * 16) * DM + col0;
; #pragma unroll
;                 for (int bj = 0; bj < 2; ++bj)
; #pragma unroll
;                     for (int n = 0; n < 2; ++n) { const f32x4 xv = *(const f32x4*)(X + ro + bj * HALF + 16 * n);
;                         *(f32x4*)(Y + ro + bj * HALF + 16 * n) = xv * DN_ALPHA + gv[bj][n] * acc[ai][bj][m][n]; } }
;     }
	v_pk_mul_f32 v[90:91], v[90:91], s[22:23] op_sel_hi:[1,0]
	v_pk_mul_f32 v[88:89], v[88:89], s[22:23] op_sel_hi:[1,0]
	v_pk_fma_f32 v[86:87], v[86:87], v[132:133], v[90:91]
	v_pk_fma_f32 v[84:85], v[84:85], v[134:135], v[88:89]
	global_store_dwordx4 v[96:97], v[84:87], off offset:512
	global_load_dwordx4 v[84:87], v[102:103], off offset:576 nt
	s_waitcnt vmcnt(0)
	v_pk_mul_f32 v[86:87], v[86:87], s[22:23] op_sel_hi:[1,0]
	v_pk_mul_f32 v[84:85], v[84:85], s[22:23] op_sel_hi:[1,0]
	v_pk_fma_f32 v[82:83], v[82:83], v[128:129], v[86:87]
	v_pk_fma_f32 v[80:81], v[80:81], v[130:131], v[84:85]
	v_lshl_add_u64 v[84:85], v[144:145], 0, s[0:1]
	global_store_dwordx4 v[96:97], v[80:83], off offset:576
	v_lshl_add_u64 v[86:87], s[4:5], 0, v[84:85]
	global_load_dwordx4 v[80:83], v[86:87], off nt
	s_mov_b64 s[0:1], 0x100000
	s_waitcnt vmcnt(0)
	v_pk_mul_f32 v[82:83], v[82:83], s[22:23] op_sel_hi:[1,0]
	v_pk_mul_f32 v[80:81], v[80:81], s[22:23] op_sel_hi:[1,0]
	v_pk_fma_f32 v[78:79], v[78:79], v[140:141], v[82:83]
	v_pk_fma_f32 v[76:77], v[76:77], v[142:143], v[80:81]
	v_lshl_add_u64 v[80:81], s[12:13], 0, v[84:85]
	global_store_dwordx4 v[80:81], v[76:79], off
	global_load_dwordx4 v[76:79], v[86:87], off offset:64 nt
	s_waitcnt vmcnt(0)
	v_pk_mul_f32 v[78:79], v[78:79], s[22:23] op_sel_hi:[1,0]
	v_pk_mul_f32 v[76:77], v[76:77], s[22:23] op_sel_hi:[1,0]
	v_pk_fma_f32 v[74:75], v[74:75], v[136:137], v[78:79]
	v_pk_fma_f32 v[72:73], v[72:73], v[138:139], v[76:77]
	global_store_dwordx4 v[80:81], v[72:75], off offset:64
	global_load_dwordx4 v[72:75], v[86:87], off offset:512 nt
	s_waitcnt vmcnt(0)
	v_pk_mul_f32 v[74:75], v[74:75], s[22:23] op_sel_hi:[1,0]
	v_pk_mul_f32 v[72:73], v[72:73], s[22:23] op_sel_hi:[1,0]
	v_pk_fma_f32 v[70:71], v[70:71], v[132:133], v[74:75]
	v_pk_fma_f32 v[68:69], v[68:69], v[134:135], v[72:73]
	global_store_dwordx4 v[80:81], v[68:71], off offset:512
	global_load_dwordx4 v[68:71], v[86:87], off offset:576 nt
	s_waitcnt vmcnt(0)
	v_pk_mul_f32 v[70:71], v[70:71], s[22:23] op_sel_hi:[1,0]
	v_pk_mul_f32 v[68:69], v[68:69], s[22:23] op_sel_hi:[1,0]
	v_pk_fma_f32 v[66:67], v[66:67], v[128:129], v[70:71]
	v_pk_fma_f32 v[64:65], v[64:65], v[130:131], v[68:69]
	v_lshl_add_u64 v[68:69], v[144:145], 0, s[0:1]
	global_store_dwordx4 v[80:81], v[64:67], off offset:576
	v_lshl_add_u64 v[70:71], s[4:5], 0, v[68:69]
	global_load_dwordx4 v[64:67], v[70:71], off nt
	s_mov_b64 s[0:1], 0x120000
	s_waitcnt vmcnt(0)
	v_pk_mul_f32 v[66:67], v[66:67], s[22:23] op_sel_hi:[1,0]
	v_pk_mul_f32 v[64:65], v[64:65], s[22:23] op_sel_hi:[1,0]
	v_pk_fma_f32 v[62:63], v[62:63], v[140:141], v[66:67]
	v_pk_fma_f32 v[60:61], v[60:61], v[142:143], v[64:65]
	v_lshl_add_u64 v[64:65], s[12:13], 0, v[68:69]
	global_store_dwordx4 v[64:65], v[60:63], off
	global_load_dwordx4 v[60:63], v[70:71], off offset:64 nt
	s_waitcnt vmcnt(0)
	v_pk_mul_f32 v[62:63], v[62:63], s[22:23] op_sel_hi:[1,0]
	v_pk_mul_f32 v[60:61], v[60:61], s[22:23] op_sel_hi:[1,0]
	v_pk_fma_f32 v[58:59], v[58:59], v[136:137], v[62:63]
	v_pk_fma_f32 v[56:57], v[56:57], v[138:139], v[60:61]
	global_store_dwordx4 v[64:65], v[56:59], off offset:64
	global_load_dwordx4 v[56:59], v[70:71], off offset:512 nt
	s_waitcnt vmcnt(0)
	v_pk_mul_f32 v[58:59], v[58:59], s[22:23] op_sel_hi:[1,0]
	v_pk_mul_f32 v[56:57], v[56:57], s[22:23] op_sel_hi:[1,0]
	v_pk_fma_f32 v[54:55], v[54:55], v[132:133], v[58:59]
	v_pk_fma_f32 v[52:53], v[52:53], v[134:135], v[56:57]
	global_store_dwordx4 v[64:65], v[52:55], off offset:512
	global_load_dwordx4 v[52:55], v[70:71], off offset:576 nt
	s_waitcnt vmcnt(0)
	v_pk_mul_f32 v[54:55], v[54:55], s[22:23] op_sel_hi:[1,0]
	v_pk_mul_f32 v[52:53], v[52:53], s[22:23] op_sel_hi:[1,0]
	v_pk_fma_f32 v[50:51], v[50:51], v[128:129], v[54:55]
	v_pk_fma_f32 v[48:49], v[48:49], v[130:131], v[52:53]
	v_lshl_add_u64 v[52:53], v[144:145], 0, s[0:1]
	global_store_dwordx4 v[64:65], v[48:51], off offset:576
	v_lshl_add_u64 v[54:55], s[4:5], 0, v[52:53]
	global_load_dwordx4 v[48:51], v[54:55], off nt
	s_mov_b64 s[0:1], 0x140000
	s_waitcnt vmcnt(0)
	v_pk_mul_f32 v[50:51], v[50:51], s[22:23] op_sel_hi:[1,0]
	v_pk_mul_f32 v[48:49], v[48:49], s[22:23] op_sel_hi:[1,0]
	v_pk_fma_f32 v[46:47], v[46:47], v[140:141], v[50:51]
	v_pk_fma_f32 v[44:45], v[44:45], v[142:143], v[48:49]
	v_lshl_add_u64 v[48:49], s[12:13], 0, v[52:53]
	global_store_dwordx4 v[48:49], v[44:47], off
	global_load_dwordx4 v[44:47], v[54:55], off offset:64 nt
	s_waitcnt vmcnt(0)
;     template <class U> __device__ __forceinline__ void operator()(const f32x4 (&acc)[2][2][4][2], const U& u, int wr, int wc, int fr, int fq) const {
;         const int row0 = u.orow0 + wr * 64 + fr, col0 = u.ocol0 + wc * 32 + 4 * fq; const int b = u.orow0 >> 12;
;         f32x4 gv[2][2];
; #pragma unroll
;         for (int bj = 0; bj < 2; ++bj)
; #pragma unroll
;             for (int n = 0; n < 2; ++n) gv[bj][n] = *(const f32x4*)(gate + (size_t)b * ADA_W + col0 + bj * HALF + 16 * n) + 1.0f;
; #pragma unroll
;         for (int ai = 0; ai < 2; ++ai)
; #pragma unroll
;             for (int m = 0; m < 4; ++m) { const size_t ro = (size_t)(row0 + ai * HALF + m * 16) * DM + col0;
; #pragma unroll
;                 for (int bj = 0; bj < 2; ++bj)
; #pragma unroll
;                     for (int n = 0; n < 2; ++n) { const f32x4 xv = *(const f32x4*)(X + ro + bj * HALF + 16 * n);
;                         *(f32x4*)(Y + ro + bj * HALF + 16 * n) = xv * DN_ALPHA + gv[bj][n] * acc[ai][bj][m][n]; } }
;     }
	v_pk_mul_f32 v[46:47], v[46:47], s[22:23] op_sel_hi:[1,0]
	v_pk_mul_f32 v[44:45], v[44:45], s[22:23] op_sel_hi:[1,0]
	v_pk_fma_f32 v[42:43], v[42:43], v[136:137], v[46:47]
	v_pk_fma_f32 v[40:41], v[40:41], v[138:139], v[44:45]
	global_store_dwordx4 v[48:49], v[40:43], off offset:64
	global_load_dwordx4 v[40:43], v[54:55], off offset:512 nt
	s_waitcnt vmcnt(0)
	v_pk_mul_f32 v[42:43], v[42:43], s[22:23] op_sel_hi:[1,0]
	v_pk_mul_f32 v[40:41], v[40:41], s[22:23] op_sel_hi:[1,0]
	v_pk_fma_f32 v[38:39], v[38:39], v[132:133], v[42:43]
	v_pk_fma_f32 v[36:37], v[36:37], v[134:135], v[40:41]
	global_store_dwordx4 v[48:49], v[36:39], off offset:512
	global_load_dwordx4 v[36:39], v[54:55], off offset:576 nt
	s_waitcnt vmcnt(0)
	v_pk_mul_f32 v[38:39], v[38:39], s[22:23] op_sel_hi:[1,0]
	v_pk_mul_f32 v[36:37], v[36:37], s[22:23] op_sel_hi:[1,0]
	v_pk_fma_f32 v[34:35], v[34:35], v[128:129], v[38:39]
	v_pk_fma_f32 v[32:33], v[32:33], v[130:131], v[36:37]
	v_lshl_add_u64 v[36:37], v[144:145], 0, s[0:1]
	global_store_dwordx4 v[48:49], v[32:35], off offset:576
	v_lshl_add_u64 v[38:39], s[4:5], 0, v[36:37]
	global_load_dwordx4 v[32:35], v[38:39], off nt
	s_mov_b64 s[0:1], 0x160000
	s_waitcnt vmcnt(0)
	v_pk_mul_f32 v[34:35], v[34:35], s[22:23] op_sel_hi:[1,0]
	v_pk_mul_f32 v[32:33], v[32:33], s[22:23] op_sel_hi:[1,0]
	v_pk_fma_f32 v[30:31], v[30:31], v[140:141], v[34:35]
	v_pk_fma_f32 v[28:29], v[28:29], v[142:143], v[32:33]
	v_lshl_add_u64 v[32:33], s[12:13], 0, v[36:37]
	global_store_dwordx4 v[32:33], v[28:31], off
	global_load_dwordx4 v[28:31], v[38:39], off offset:64 nt
	s_waitcnt vmcnt(0)
	v_pk_mul_f32 v[30:31], v[30:31], s[22:23] op_sel_hi:[1,0]
	v_pk_mul_f32 v[28:29], v[28:29], s[22:23] op_sel_hi:[1,0]
	v_pk_fma_f32 v[26:27], v[26:27], v[136:137], v[30:31]
	v_pk_fma_f32 v[24:25], v[24:25], v[138:139], v[28:29]
	global_store_dwordx4 v[32:33], v[24:27], off offset:64
	global_load_dwordx4 v[24:27], v[38:39], off offset:512 nt
	s_waitcnt vmcnt(0)
	v_pk_mul_f32 v[26:27], v[26:27], s[22:23] op_sel_hi:[1,0]
	v_pk_mul_f32 v[24:25], v[24:25], s[22:23] op_sel_hi:[1,0]
	v_pk_fma_f32 v[22:23], v[22:23], v[132:133], v[26:27]
	v_pk_fma_f32 v[20:21], v[20:21], v[134:135], v[24:25]
	global_store_dwordx4 v[32:33], v[20:23], off offset:512
	global_load_dwordx4 v[20:23], v[38:39], off offset:576 nt
	s_waitcnt vmcnt(0)
	v_pk_mul_f32 v[22:23], v[22:23], s[22:23] op_sel_hi:[1,0]
	v_pk_mul_f32 v[20:21], v[20:21], s[22:23] op_sel_hi:[1,0]
	v_pk_fma_f32 v[18:19], v[18:19], v[128:129], v[22:23]
	v_pk_fma_f32 v[16:17], v[16:17], v[130:131], v[20:21]
	v_lshl_add_u64 v[20:21], v[144:145], 0, s[0:1]
	global_store_dwordx4 v[32:33], v[16:19], off offset:576
	v_lshl_add_u64 v[22:23], s[4:5], 0, v[20:21]
	global_load_dwordx4 v[16:19], v[22:23], off nt
	s_waitcnt vmcnt(0)
	v_pk_mul_f32 v[18:19], v[18:19], s[22:23] op_sel_hi:[1,0]
	v_pk_mul_f32 v[16:17], v[16:17], s[22:23] op_sel_hi:[1,0]
	v_pk_fma_f32 v[14:15], v[14:15], v[140:141], v[18:19]
	v_pk_fma_f32 v[12:13], v[12:13], v[142:143], v[16:17]
	v_lshl_add_u64 v[16:17], s[12:13], 0, v[20:21]
	global_store_dwordx4 v[16:17], v[12:15], off
	global_load_dwordx4 v[12:15], v[22:23], off offset:64 nt
	s_waitcnt vmcnt(0)
	v_pk_mul_f32 v[14:15], v[14:15], s[22:23] op_sel_hi:[1,0]
	v_pk_mul_f32 v[12:13], v[12:13], s[22:23] op_sel_hi:[1,0]
	v_pk_fma_f32 v[10:11], v[10:11], v[136:137], v[14:15]
	v_pk_fma_f32 v[8:9], v[8:9], v[138:139], v[12:13]
	global_store_dwordx4 v[16:17], v[8:11], off offset:64
	global_load_dwordx4 v[8:11], v[22:23], off offset:512 nt
	s_waitcnt vmcnt(0)
	v_pk_mul_f32 v[10:11], v[10:11], s[22:23] op_sel_hi:[1,0]
	v_pk_mul_f32 v[8:9], v[8:9], s[22:23] op_sel_hi:[1,0]
	v_pk_fma_f32 v[6:7], v[6:7], v[132:133], v[10:11]
	v_pk_fma_f32 v[4:5], v[4:5], v[134:135], v[8:9]
	global_store_dwordx4 v[16:17], v[4:7], off offset:512
	global_load_dwordx4 v[4:7], v[22:23], off offset:576 nt
	s_waitcnt vmcnt(0)
	v_pk_mul_f32 v[6:7], v[6:7], s[22:23] op_sel_hi:[1,0]
	v_pk_mul_f32 v[4:5], v[4:5], s[22:23] op_sel_hi:[1,0]
	v_pk_fma_f32 v[2:3], v[2:3], v[128:129], v[6:7]
	v_pk_fma_f32 v[0:1], v[0:1], v[130:131], v[4:5]
	global_store_dwordx4 v[16:17], v[0:3], off offset:576
	s_cbranch_vccnz .LBB0_984
